# short-conv row loop: all tap loads issued together at the row head, filter/mixg fragments with the first loads of the row, counted waits (4 load->wait round trips per row -> 2)
# speedup vs baseline: 1.0044x; 1.0011x over previous
; __device__ __forceinline__ unsigned pk2(float lo, float hi) { return hw_pk_bf16(lo, hi); }
; __device__ __forceinline__ void conv_row(const Frame& F, const bf16* __restrict__ proj, const float* cw, const float* mixg, bf16* mix, int t) {
;     ...
;     for (int k = 0; k < 3; ++k) { const int tt = t - 2 + k;
;         if (tt >= 0) { const u32x4 a = *(const u32x4*)(proj + (size_t)tt * PW + C_CC + c0), b = *(const u32x4*)(proj + (size_t)tt * PW + C_CH + c0);
;             z[k][0] = bflo(a.x) * bflo(b.x); z[k][1] = bfhi(a.x) * bfhi(b.x); z[k][2] = bflo(a.y) * bflo(b.y); z[k][3] = bfhi(a.y) * bfhi(b.y);
;             z[k][4] = bflo(a.z) * bflo(b.z); z[k][5] = bfhi(a.z) * bfhi(b.z); z[k][6] = bflo(a.w) * bflo(b.w); z[k][7] = bfhi(a.w) * bfhi(b.w); }
;         else {
; #pragma unroll
;             for (int j = 0; j < 8; ++j) z[k][j] = 0.f; } }
;     const u32x4 bb = *(const u32x4*)(proj + (size_t)t * PW + C_CB + c0);
;     const float bv[8] = {bflo(bb.x), bfhi(bb.x), bflo(bb.y), bfhi(bb.y), bflo(bb.z), bfhi(bb.z), bflo(bb.w), bfhi(bb.w)};
;     float o[8]; float ss = 0.f;
; #pragma unroll
;     for (int j = 0; j < 8; ++j) { const float cv = cw[c0 + j] * z[0][j] + cw[GW + c0 + j] * z[1][j] + cw[2 * GW + c0 + j] * z[2][j]; o[j] = bv[j] * cv; ss += o[j] * o[j]; }
;     ss = wave_sum(ss);
;     const float rstd = rsqrtf(ss * (1.0f / 512.0f) + EPS);
;     u32x4 wv; wv.x = pk2(o[0] * rstd * mixg[c0], o[1] * rstd * mixg[c0 + 1]); wv.y = pk2(o[2] * rstd * mixg[c0 + 2], o[3] * rstd * mixg[c0 + 3]);
;     wv.z = pk2(o[4] * rstd * mixg[c0 + 4], o[5] * rstd * mixg[c0 + 5]); wv.w = pk2(o[6] * rstd * mixg[c0 + 6], o[7] * rstd * mixg[c0 + 7]);
;     *(u32x4*)(mix + (size_t)t * D + 512 + c0) = wv;
.LBB0_425:
	s_waitcnt vmcnt(1)
	v_mov_b64_e32 v[20:21], v[90:91]
	v_mov_b64_e32 v[22:23], v[92:93]
	v_and_b32_e32 v12, 0xffff0000, v20
	v_lshlrev_b32_e32 v13, 16, v20
	s_waitcnt vmcnt(0)
	v_mov_b64_e32 v[24:25], v[94:95]
	v_mov_b64_e32 v[26:27], v[96:97]
	v_and_b32_e32 v28, 0xffff0000, v24
	v_lshlrev_b32_e32 v29, 16, v24
	v_and_b32_e32 v20, 0xffff0000, v21
	v_lshlrev_b32_e32 v21, 16, v21
	v_and_b32_e32 v24, 0xffff0000, v25
	v_lshlrev_b32_e32 v25, 16, v25
	v_pk_mul_f32 v[12:13], v[12:13], v[28:29]
	v_pk_mul_f32 v[20:21], v[20:21], v[24:25]
	v_and_b32_e32 v24, 0xffff0000, v22
	v_lshlrev_b32_e32 v25, 16, v22
	v_and_b32_e32 v28, 0xffff0000, v26
	v_lshlrev_b32_e32 v29, 16, v26
	v_pk_mul_f32 v[28:29], v[24:25], v[28:29]
	v_and_b32_e32 v22, 0xffff0000, v23
	v_lshlrev_b32_e32 v23, 16, v23
	v_and_b32_e32 v24, 0xffff0000, v27
	v_lshlrev_b32_e32 v25, 16, v27
	v_pk_mul_f32 v[22:23], v[22:23], v[24:25]
	v_mov_b32_e32 v24, v29
	v_mov_b32_e32 v26, v23
	v_mov_b32_e32 v27, v22
	v_mov_b32_e32 v25, v28
	v_mov_b32_e32 v22, v21
	v_mov_b32_e32 v23, v20
	v_mov_b32_e32 v20, v13
	v_mov_b32_e32 v21, v12
.LBB0_426:
	v_lshlrev_b64 v[12:13], 1, v[10:11]
	v_lshlrev_b64 v[10:11], 2, v[10:11]
	v_lshl_add_u64 v[28:29], s[48:49], 0, v[12:13]
	v_lshl_add_u64 v[48:49], s[8:9], 0, v[10:11]
	global_load_dwordx4 v[28:31], v[28:29], off
	s_nop 0
	global_load_dwordx4 v[32:35], v[48:49], off offset:16
	global_load_dwordx4 v[36:39], v[48:49], off
	global_load_dwordx4 v[40:43], v[48:49], off offset:2064
	global_load_dwordx4 v[44:47], v[48:49], off offset:2048
	v_lshl_add_u64 v[50:51], v[48:49], 0, s[66:67]
	v_lshl_add_u64 v[10:11], s[10:11], 0, v[10:11]
	v_add_co_u32_e32 v72, vcc, s25, v48
	s_nop 1
	v_addc_co_u32_e32 v73, vcc, 0, v49, vcc
	global_load_dwordx4 v[64:67], v[72:73], off
	global_load_dwordx4 v[68:71], v[50:51], off offset:16
	global_load_dwordx4 v[56:59], v[10:11], off offset:2064
	global_load_dwordx4 v[60:63], v[10:11], off offset:2048
	s_add_i32 s4, s4, s6
	s_waitcnt vmcnt(5)
	v_pk_mul_f32 v[16:17], v[16:17], v[42:43]
	s_nop 0
	v_pk_fma_f32 v[34:35], v[18:19], v[34:35], v[16:17]
	s_waitcnt vmcnt(4)
	v_pk_mul_f32 v[8:9], v[8:9], v[46:47]
	v_pk_mul_f32 v[6:7], v[6:7], v[44:45]
	v_pk_mul_f32 v[14:15], v[14:15], v[40:41]
	v_pk_fma_f32 v[2:3], v[2:3], v[38:39], v[8:9]
	v_pk_fma_f32 v[0:1], v[0:1], v[36:37], v[6:7]
	v_pk_fma_f32 v[4:5], v[4:5], v[32:33], v[14:15]
	v_lshlrev_b32_e32 v42, 16, v30
	v_and_b32_e32 v43, 0xffff0000, v30
	v_lshlrev_b32_e32 v52, 16, v31
	v_and_b32_e32 v53, 0xffff0000, v31
	s_waitcnt vmcnt(3)
	v_pk_fma_f32 v[2:3], v[22:23], v[66:67], v[2:3]
	v_lshlrev_b32_e32 v18, 16, v28
	v_and_b32_e32 v19, 0xffff0000, v28
	v_pk_fma_f32 v[0:1], v[20:21], v[64:65], v[0:1]
	s_waitcnt vmcnt(2)
	v_pk_fma_f32 v[4:5], v[24:25], v[68:69], v[4:5]
	v_lshlrev_b32_e32 v24, 16, v29
	v_and_b32_e32 v25, 0xffff0000, v29
	v_pk_mul_f32 v[0:1], v[0:1], v[18:19]
	v_pk_mul_f32 v[8:9], v[2:3], v[24:25]
	v_pk_mul_f32 v[6:7], v[0:1], v[0:1]
	v_pk_mul_f32 v[2:3], v[8:9], v[8:9]
	v_add_f32_e32 v6, v6, v7
	v_pk_mul_f32 v[14:15], v[4:5], v[42:43]
	v_add_f32_e32 v2, v6, v2
	v_pk_fma_f32 v[26:27], v[26:27], v[70:71], v[34:35]
	v_pk_mul_f32 v[4:5], v[14:15], v[14:15]
	v_add_f32_e32 v2, v2, v3
	v_pk_mul_f32 v[26:27], v[26:27], v[52:53]
	v_add_f32_e32 v2, v2, v4
	v_pk_mul_f32 v[34:35], v[26:27], v[26:27]
	v_add_f32_e32 v2, v2, v5
	v_add_f32_e32 v2, v2, v34
	v_add_f32_e32 v2, v2, v35
	s_nop 1
	v_add_f32_dpp v2, v2, v2 quad_perm:[1,0,3,2] row_mask:0xf bank_mask:0xf bound_ctrl:1
	s_nop 1
	v_add_f32_dpp v2, v2, v2 quad_perm:[2,3,0,1] row_mask:0xf bank_mask:0xf bound_ctrl:1
	s_nop 1
	v_add_f32_dpp v2, v2, v2 row_half_mirror row_mask:0xf bank_mask:0xf bound_ctrl:1
	s_nop 1
	v_add_f32_dpp v2, v2, v2 row_mirror row_mask:0xf bank_mask:0xf bound_ctrl:1
	v_mov_b32_e32 v3, v2
	s_nop 1
	v_permlane32_swap_b32 v3, v2
	s_nop 0
	v_add_f32_e32 v2, v3, v2
	s_nop 0
	v_readlane_b32 s7, v2, 16
	v_readlane_b32 s5, v2, 0
	s_nop 0
	v_mov_b32_e32 v2, s7
	v_add_f32_e32 v2, s5, v2
	v_fmamk_f32 v2, v2, 0x3b000000, v194
	v_cmp_gt_f32_e32 vcc, s26, v2
	v_mul_f32_e32 v3, 0x4b800000, v2
	s_mul_i32 s5, s6, 0x2400
	v_cndmask_b32_e32 v2, v2, v3, vcc
	v_rsq_f32_e32 v2, v2
	s_nop 0
	v_mul_f32_e32 v3, 0x45800000, v2
	v_cndmask_b32_e32 v16, v2, v3, vcc
	v_pk_mul_f32 v[18:19], v[0:1], v[16:17] op_sel_hi:[1,0]
	v_pk_mul_f32 v[8:9], v[8:9], v[16:17] op_sel_hi:[1,0]
	s_waitcnt vmcnt(0)
	v_pk_mul_f32 v[4:5], v[60:61], v[18:19]
	v_pk_mul_f32 v[6:7], v[62:63], v[8:9]
	v_cvt_pk_bf16_f32 v4, v4, v5
	v_cvt_pk_bf16_f32 v5, v6, v7
	v_pk_mul_f32 v[6:7], v[14:15], v[16:17] op_sel_hi:[1,0]
	s_nop 0
	v_pk_mul_f32 v[0:1], v[56:57], v[6:7]
	s_nop 0
	v_cvt_pk_bf16_f32 v6, v0, v1
	v_pk_mul_f32 v[0:1], v[26:27], v[16:17] op_sel_hi:[1,0]
	s_nop 0
	v_pk_mul_f32 v[0:1], v[58:59], v[0:1]
	s_nop 0
	v_cvt_pk_bf16_f32 v7, v0, v1
	v_lshl_add_u64 v[0:1], s[38:39], 0, v[12:13]
	s_add_u32 s38, s38, s42
	s_addc_u32 s39, s39, s43
	s_add_u32 s48, s48, s5
	s_mul_hi_i32 s5, s6, 0x2400
	s_addc_u32 s49, s49, s5
	s_cmp_ge_i32 s4, s13
	global_store_dwordx4 v[0:1], v[4:7], off
	s_cbranch_scc1 .LBB0_433
; __device__ __forceinline__ void conv_row(const Frame& F, const bf16* __restrict__ proj, const float* cw, const float* mixg, bf16* mix, int t) {
;     ...
;     for (int k = 0; k < 3; ++k) { const int tt = t - 2 + k;
;         if (tt >= 0) { const u32x4 a = *(const u32x4*)(proj + (size_t)tt * PW + C_CC + c0), b = *(const u32x4*)(proj + (size_t)tt * PW + C_CH + c0);
;             z[k][0] = bflo(a.x) * bflo(b.x); z[k][1] = bfhi(a.x) * bfhi(b.x); z[k][2] = bflo(a.y) * bflo(b.y); z[k][3] = bfhi(a.y) * bfhi(b.y);
;             z[k][4] = bflo(a.z) * bflo(b.z); z[k][5] = bfhi(a.z) * bfhi(b.z); z[k][6] = bflo(a.w) * bflo(b.w); z[k][7] = bfhi(a.w) * bfhi(b.w); }
;         else {
; #pragma unroll
;             for (int j = 0; j < 8; ++j) z[k][j] = 0.f; } }
.LBB0_427:
	s_nop 1
	v_mov_b32_e32 v0, v193
	v_mov_b32_e32 v16, 0
	v_mbcnt_lo_u32_b32 v0, -1, v0
	v_mbcnt_hi_u32_b32 v0, -1, v0
	s_cmp_lt_i32 s4, 2
	v_lshlrev_b32_e32 v10, 3, v0
	v_ashrrev_i32_e32 v11, 31, v10
	v_mov_b32_e32 v18, 0
	v_mov_b32_e32 v19, 0
	v_mov_b32_e32 v4, 0
	v_mov_b32_e32 v5, 0
	v_mov_b32_e32 v2, 0
	v_mov_b32_e32 v3, 0
	v_mov_b32_e32 v0, 0
	v_mov_b32_e32 v1, 0
	s_max_i32 s5, s4, 0
	s_mul_hi_u32 s7, s5, 0x2400
	s_mulk_i32 s5, 0x2400
	s_add_u32 s30, s44, s5
	s_addc_u32 s31, s45, s7
	v_lshl_add_u64 v[102:103], v[10:11], 1, s[30:31]
	s_cmp_lt_i32 s4, 1
	s_cselect_b32 s5, 0, 0x2400
	s_sub_u32 s30, s30, s5
	s_subb_u32 s31, s31, 0
	v_lshl_add_u64 v[100:101], v[10:11], 1, s[30:31]
	s_cmp_lt_i32 s4, 2
	s_cselect_b32 s5, 0, 0x2400
	s_sub_u32 s30, s30, s5
	s_subb_u32 s31, s31, 0
	v_lshl_add_u64 v[98:99], v[10:11], 1, s[30:31]
	global_load_dwordx4 v[74:77], v[98:99], off offset:2048
	global_load_dwordx4 v[78:81], v[98:99], off offset:3072
	global_load_dwordx4 v[82:85], v[100:101], off offset:2048
	global_load_dwordx4 v[86:89], v[100:101], off offset:3072
	global_load_dwordx4 v[90:93], v[102:103], off offset:2048
	global_load_dwordx4 v[94:97], v[102:103], off offset:3072
	s_cmp_lt_i32 s4, 2
	s_cbranch_scc1 .LBB0_429
	s_waitcnt vmcnt(5)
	v_mov_b64_e32 v[4:5], v[74:75]
	v_mov_b64_e32 v[6:7], v[76:77]
	v_lshlrev_b32_e32 v0, 16, v4
	v_and_b32_e32 v1, 0xffff0000, v4
	s_waitcnt vmcnt(4)
	v_mov_b64_e32 v[12:13], v[78:79]
	v_mov_b64_e32 v[14:15], v[80:81]
	v_lshlrev_b32_e32 v2, 16, v12
	v_and_b32_e32 v3, 0xffff0000, v12
	v_pk_mul_f32 v[0:1], v[0:1], v[2:3]
	v_lshlrev_b32_e32 v2, 16, v5
	v_and_b32_e32 v3, 0xffff0000, v5
	v_lshlrev_b32_e32 v4, 16, v13
	v_and_b32_e32 v5, 0xffff0000, v13
	v_pk_mul_f32 v[2:3], v[2:3], v[4:5]
	v_lshlrev_b32_e32 v4, 16, v6
	v_and_b32_e32 v5, 0xffff0000, v6
	v_lshlrev_b32_e32 v8, 16, v14
	v_and_b32_e32 v9, 0xffff0000, v14
	v_pk_mul_f32 v[4:5], v[4:5], v[8:9]
	v_lshlrev_b32_e32 v6, 16, v7
	v_and_b32_e32 v7, 0xffff0000, v7
	v_lshlrev_b32_e32 v8, 16, v15
	v_and_b32_e32 v9, 0xffff0000, v15
	v_pk_mul_f32 v[18:19], v[6:7], v[8:9]
.LBB0_429:
	s_cmp_lt_i32 s4, 1
	v_mov_b32_e32 v17, 0
	v_mov_b32_e32 v14, 0
	v_mov_b32_e32 v15, 0
	v_mov_b32_e32 v8, 0
	v_mov_b32_e32 v9, 0
	v_mov_b32_e32 v6, 0
	v_mov_b32_e32 v7, 0
	s_cbranch_scc1 .LBB0_431
	s_waitcnt vmcnt(3)
	v_mov_b64_e32 v[14:15], v[82:83]
	v_mov_b64_e32 v[16:17], v[84:85]
	v_lshlrev_b32_e32 v6, 16, v14
	v_and_b32_e32 v7, 0xffff0000, v14
	s_waitcnt vmcnt(2)
	v_mov_b64_e32 v[20:21], v[86:87]
	v_mov_b64_e32 v[22:23], v[88:89]
	v_lshlrev_b32_e32 v8, 16, v20
	v_and_b32_e32 v9, 0xffff0000, v20
	v_pk_mul_f32 v[6:7], v[6:7], v[8:9]
	v_lshlrev_b32_e32 v8, 16, v15
	v_and_b32_e32 v9, 0xffff0000, v15
	v_lshlrev_b32_e32 v12, 16, v21
	v_and_b32_e32 v13, 0xffff0000, v21
	v_pk_mul_f32 v[8:9], v[8:9], v[12:13]
	v_lshlrev_b32_e32 v12, 16, v16
	v_and_b32_e32 v13, 0xffff0000, v16
	v_lshlrev_b32_e32 v14, 16, v22
	v_and_b32_e32 v15, 0xffff0000, v22
	v_pk_mul_f32 v[14:15], v[12:13], v[14:15]
	v_lshlrev_b32_e32 v12, 16, v17
	v_and_b32_e32 v13, 0xffff0000, v17
	v_lshlrev_b32_e32 v16, 16, v23
	v_and_b32_e32 v17, 0xffff0000, v23
	v_pk_mul_f32 v[16:17], v[12:13], v[16:17]
